# router K-loop: path-specific vmcnt ladder (do not drain the loads just issued); plus P1 and combine next-row touch prefetch
# baseline (speedup 1.0000x reference)
;     ...
;         bf16x8 xhA[4], xlA[4], whA[4], wlA[4], xhB[4], xlB[4], whB[4], wlB[4];
;         RT_LOAD(xhA, xlA, whA, wlA, 0);
;         for (int ks = 0; ks < 32; ks += 2) {
;             RT_LOAD(xhB, xlB, whB, wlB, (ks + 1) * 32);
;             RT_MMA(xhA, xlA, whA, wlA);
;             if (ks + 2 < 32) RT_LOAD(xhA, xlA, whA, wlA, (ks + 2) * 32);
;             RT_MMA(xhB, xlB, whB, wlB);
;         }
.Lrt_join_a:
	v_mfma_f32_16x16x32_bf16 v[118:121], v[142:145], v[126:129], v[118:121]
	v_mfma_f32_16x16x32_bf16 v[114:117], v[90:93], v[162:165], v[114:117]
	v_mfma_f32_16x16x32_bf16 v[122:125], v[90:93], v[70:73], v[122:125]
	v_mfma_f32_16x16x32_bf16 v[102:105], v[90:93], v[66:69], v[102:105]
	v_mfma_f32_16x16x32_bf16 v[142:145], v[90:93], v[182:185], v[150:153]
	v_mfma_f32_16x16x32_bf16 v[114:117], v[138:141], v[162:165], v[114:117]
	v_mfma_f32_16x16x32_bf16 v[122:125], v[138:141], v[70:73], v[122:125]
	v_mfma_f32_16x16x32_bf16 v[102:105], v[138:141], v[66:69], v[102:105]
	v_mfma_f32_16x16x32_bf16 v[138:141], v[138:141], v[182:185], v[142:145]
	v_mfma_f32_16x16x32_bf16 v[82:85], v[154:157], v[70:73], v[82:85]
	v_mfma_f32_16x16x32_bf16 v[114:117], v[90:93], v[166:169], v[114:117]
	v_mfma_f32_16x16x32_bf16 v[122:125], v[90:93], v[170:173], v[122:125]
	v_mfma_f32_16x16x32_bf16 v[102:105], v[90:93], v[178:181], v[102:105]
	v_mfma_f32_16x16x32_bf16 v[90:93], v[90:93], v[126:129], v[138:141]
	v_mfma_f32_16x16x32_bf16 v[138:141], v[130:133], v[70:73], v[174:177]
	v_mfma_f32_16x16x32_bf16 v[82:85], v[158:161], v[70:73], v[82:85]
	v_mfma_f32_16x16x32_bf16 v[86:89], v[154:157], v[66:69], v[86:89]
	v_mfma_f32_16x16x32_bf16 v[70:73], v[134:137], v[70:73], v[138:141]
	v_mfma_f32_16x16x32_bf16 v[138:141], v[130:133], v[66:69], v[186:189]
	v_mfma_f32_16x16x32_bf16 v[78:81], v[154:157], v[162:165], v[78:81]
	v_mfma_f32_16x16x32_bf16 v[86:89], v[158:161], v[66:69], v[86:89]
	v_mfma_f32_16x16x32_bf16 v[98:101], v[154:157], v[182:185], v[98:101]
	v_mfma_f32_16x16x32_bf16 v[74:77], v[130:133], v[162:165], v[74:77]
	v_mfma_f32_16x16x32_bf16 v[66:69], v[134:137], v[66:69], v[138:141]
	v_mfma_f32_16x16x32_bf16 v[138:141], v[130:133], v[182:185], v[190:193]
	v_mfma_f32_16x16x32_bf16 v[78:81], v[158:161], v[162:165], v[78:81]
	v_mfma_f32_16x16x32_bf16 v[98:101], v[158:161], v[182:185], v[98:101]
	v_mfma_f32_16x16x32_bf16 v[74:77], v[134:137], v[162:165], v[74:77]
	v_mfma_f32_16x16x32_bf16 v[134:137], v[134:137], v[182:185], v[138:141]
	v_mfma_f32_16x16x32_bf16 v[78:81], v[154:157], v[166:169], v[78:81]
	v_mfma_f32_16x16x32_bf16 v[82:85], v[154:157], v[170:173], v[82:85]
	v_mfma_f32_16x16x32_bf16 v[86:89], v[154:157], v[178:181], v[86:89]
	v_mfma_f32_16x16x32_bf16 v[98:101], v[154:157], v[126:129], v[98:101]
	v_mfma_f32_16x16x32_bf16 v[74:77], v[130:133], v[166:169], v[74:77]
	v_mfma_f32_16x16x32_bf16 v[70:73], v[130:133], v[170:173], v[70:73]
	v_mfma_f32_16x16x32_bf16 v[66:69], v[130:133], v[178:181], v[66:69]
	v_mfma_f32_16x16x32_bf16 v[126:129], v[130:133], v[126:129], v[134:137]
	s_cbranch_vccnz .LBB0_662
.LBB0_660:
	v_lshl_add_u64 v[228:229], s[38:39], 0, v[222:223]
	v_add_co_u32_e32 v130, vcc, s44, v228
	v_lshl_add_u64 v[226:227], s[38:39], 0, v[224:225]
	s_nop 0
	v_addc_co_u32_e32 v131, vcc, 0, v229, vcc
	v_add_co_u32_e32 v132, vcc, s45, v228
	s_waitcnt vmcnt(0)
	v_mfma_f32_16x16x32_bf16 v[182:185], v[26:29], v[50:53], v[66:69]
	v_addc_co_u32_e32 v133, vcc, 0, v229, vcc
	global_load_dwordx4 v[154:157], v[130:131], off offset:64
	global_load_dwordx4 v[158:161], v[132:133], off offset:64 nt
	v_add_co_u32_e32 v130, vcc, s46, v228
	v_mfma_f32_16x16x32_bf16 v[70:73], v[26:29], v[42:45], v[70:73]
	s_nop 0
	v_addc_co_u32_e32 v131, vcc, 0, v229, vcc
	v_add_co_u32_e32 v132, vcc, s47, v228
	v_mfma_f32_16x16x32_bf16 v[182:185], v[30:33], v[50:53], v[182:185]
	s_nop 0
	v_addc_co_u32_e32 v133, vcc, 0, v229, vcc
	v_add_co_u32_e32 v134, vcc, s48, v228
	global_load_dwordx4 v[142:145], v[130:131], off offset:64
	global_load_dwordx4 v[146:149], v[132:133], off offset:64 nt
	v_addc_co_u32_e32 v135, vcc, 0, v229, vcc
	v_add_co_u32_e32 v136, vcc, s49, v228
	v_mfma_f32_16x16x32_bf16 v[130:133], v[18:21], v[58:61], v[90:93]
	s_nop 0
	v_addc_co_u32_e32 v137, vcc, 0, v229, vcc
	s_nop 0
	global_load_dwordx4 v[90:93], v[134:135], off offset:64
	global_load_dwordx4 v[138:141], v[136:137], off offset:64 nt
	v_add_co_u32_e32 v134, vcc, s50, v228
	v_mfma_f32_16x16x32_bf16 v[130:133], v[22:25], v[58:61], v[130:133]
	s_nop 0
	v_addc_co_u32_e32 v135, vcc, 0, v229, vcc
	v_add_co_u32_e32 v136, vcc, s51, v228
	v_mfma_f32_16x16x32_bf16 v[150:153], v[18:21], v[62:65], v[130:133]
	s_nop 0
	v_addc_co_u32_e32 v137, vcc, 0, v229, vcc
	v_add_co_u32_e32 v162, vcc, s52, v226
	s_nop 0
	global_load_dwordx4 v[130:133], v[134:135], off offset:64
	s_nop 0
	global_load_dwordx4 v[134:137], v[136:137], off offset:64 nt
	v_addc_co_u32_e32 v163, vcc, 0, v227, vcc
	v_add_co_u32_e32 v166, vcc, s53, v226
	v_mfma_f32_16x16x32_bf16 v[174:177], v[30:33], v[42:45], v[70:73]
	s_nop 0
	v_addc_co_u32_e32 v167, vcc, 0, v227, vcc
	v_add_co_u32_e32 v170, vcc, s54, v226
	global_load_dwordx4 v[162:165], v[162:163], off offset:64
	s_nop 0
	global_load_dwordx4 v[166:169], v[166:167], off offset:64
	v_addc_co_u32_e32 v171, vcc, 0, v227, vcc
	v_add_co_u32_e32 v172, vcc, s55, v226
	v_mfma_f32_16x16x32_bf16 v[186:189], v[26:29], v[54:57], v[182:185]
	s_nop 0
	v_addc_co_u32_e32 v173, vcc, 0, v227, vcc
	v_add_co_u32_e32 v178, vcc, s56, v226
	global_load_dwordx4 v[70:73], v[170:171], off offset:64
	s_nop 0
	global_load_dwordx4 v[170:173], v[172:173], off offset:64
	v_addc_co_u32_e32 v179, vcc, 0, v227, vcc
	v_add_co_u32_e32 v180, vcc, s57, v226
	v_mfma_f32_16x16x32_bf16 v[190:193], v[26:29], v[58:61], v[126:129]
	s_nop 0
	v_addc_co_u32_e32 v181, vcc, 0, v227, vcc
	v_add_co_u32_e32 v238, vcc, s58, v226
	global_load_dwordx4 v[66:69], v[178:179], off offset:64
	s_nop 0
	global_load_dwordx4 v[178:181], v[180:181], off offset:64
	v_addc_co_u32_e32 v239, vcc, 0, v227, vcc
	v_add_co_u32_e32 v240, vcc, s59, v226
;     ...
;         bf16x8 xhA[4], xlA[4], whA[4], wlA[4], xhB[4], xlB[4], whB[4], wlB[4];
;         RT_LOAD(xhA, xlA, whA, wlA, 0);
;         for (int ks = 0; ks < 32; ks += 2) {
;             RT_LOAD(xhB, xlB, whB, wlB, (ks + 1) * 32);
;             RT_MMA(xhA, xlA, whA, wlA);
;             if (ks + 2 < 32) RT_LOAD(xhA, xlA, whA, wlA, (ks + 2) * 32);
;             RT_MMA(xhB, xlB, whB, wlB);
;         }
	v_mfma_f32_16x16x32_bf16 v[78:81], v[2:5], v[34:37], v[78:81]
	s_nop 0
	v_addc_co_u32_e32 v241, vcc, 0, v227, vcc
	global_load_dwordx4 v[182:185], v[238:239], off offset:64
	global_load_dwordx4 v[126:129], v[240:241], off offset:64
	v_mfma_f32_16x16x32_bf16 v[82:85], v[2:5], v[42:45], v[82:85]
	s_cmp_gt_u32 s20, 29
	s_cselect_b64 s[18:19], -1, 0
	s_and_b64 vcc, exec, s[18:19]
	v_mfma_f32_16x16x32_bf16 v[86:89], v[2:5], v[50:53], v[86:89]
	v_mfma_f32_16x16x32_bf16 v[98:101], v[2:5], v[58:61], v[98:101]
	v_mfma_f32_16x16x32_bf16 v[94:97], v[10:13], v[34:37], v[94:97]
	v_mfma_f32_16x16x32_bf16 v[110:113], v[10:13], v[42:45], v[110:113]
	v_mfma_f32_16x16x32_bf16 v[106:109], v[10:13], v[50:53], v[106:109]
	v_mfma_f32_16x16x32_bf16 v[118:121], v[10:13], v[58:61], v[118:121]
	v_mfma_f32_16x16x32_bf16 v[114:117], v[18:21], v[34:37], v[114:117]
	v_mfma_f32_16x16x32_bf16 v[122:125], v[18:21], v[42:45], v[122:125]
	v_mfma_f32_16x16x32_bf16 v[102:105], v[18:21], v[50:53], v[102:105]
	v_mfma_f32_16x16x32_bf16 v[74:77], v[26:29], v[34:37], v[74:77]
	v_mfma_f32_16x16x32_bf16 v[78:81], v[6:9], v[34:37], v[78:81]
	v_mfma_f32_16x16x32_bf16 v[82:85], v[6:9], v[42:45], v[82:85]
	v_mfma_f32_16x16x32_bf16 v[86:89], v[6:9], v[50:53], v[86:89]
	v_mfma_f32_16x16x32_bf16 v[98:101], v[6:9], v[58:61], v[98:101]
	v_mfma_f32_16x16x32_bf16 v[94:97], v[14:17], v[34:37], v[94:97]
	v_mfma_f32_16x16x32_bf16 v[110:113], v[14:17], v[42:45], v[110:113]
	v_mfma_f32_16x16x32_bf16 v[106:109], v[14:17], v[50:53], v[106:109]
	v_mfma_f32_16x16x32_bf16 v[118:121], v[14:17], v[58:61], v[118:121]
	v_mfma_f32_16x16x32_bf16 v[114:117], v[22:25], v[34:37], v[114:117]
	v_mfma_f32_16x16x32_bf16 v[122:125], v[22:25], v[42:45], v[122:125]
	v_mfma_f32_16x16x32_bf16 v[102:105], v[22:25], v[50:53], v[102:105]
	v_mfma_f32_16x16x32_bf16 v[74:77], v[30:33], v[34:37], v[74:77]
	v_mfma_f32_16x16x32_bf16 v[190:193], v[30:33], v[58:61], v[190:193]
	v_mfma_f32_16x16x32_bf16 v[78:81], v[2:5], v[38:41], v[78:81]
	v_mfma_f32_16x16x32_bf16 v[82:85], v[2:5], v[46:49], v[82:85]
	v_mfma_f32_16x16x32_bf16 v[86:89], v[2:5], v[54:57], v[86:89]
	v_mfma_f32_16x16x32_bf16 v[98:101], v[2:5], v[62:65], v[98:101]
	v_mfma_f32_16x16x32_bf16 v[94:97], v[10:13], v[38:41], v[94:97]
	v_mfma_f32_16x16x32_bf16 v[110:113], v[10:13], v[46:49], v[110:113]
	v_mfma_f32_16x16x32_bf16 v[106:109], v[10:13], v[54:57], v[106:109]
	v_mfma_f32_16x16x32_bf16 v[118:121], v[10:13], v[62:65], v[118:121]
	v_mfma_f32_16x16x32_bf16 v[114:117], v[18:21], v[38:41], v[114:117]
	v_mfma_f32_16x16x32_bf16 v[122:125], v[18:21], v[46:49], v[122:125]
	v_mfma_f32_16x16x32_bf16 v[102:105], v[18:21], v[54:57], v[102:105]
	v_mfma_f32_16x16x32_bf16 v[74:77], v[26:29], v[38:41], v[74:77]
	v_mfma_f32_16x16x32_bf16 v[174:177], v[26:29], v[46:49], v[174:177]
	v_mfma_f32_16x16x32_bf16 v[190:193], v[26:29], v[62:65], v[190:193]
	s_cbranch_vccnz .LBB0_659
	v_add_co_u32_e32 v2, vcc, 0x8800000, v228
	s_nop 1
	v_addc_co_u32_e32 v3, vcc, 0, v229, vcc
	v_add_co_u32_e32 v6, vcc, 0x14c00000, v228
	s_nop 1
	v_addc_co_u32_e32 v7, vcc, 0, v229, vcc
	v_add_co_u32_e32 v10, vcc, 0x8808000, v228
	global_load_dwordx4 v[2:5], v[2:3], off offset:128
	s_nop 0
	global_load_dwordx4 v[6:9], v[6:7], off offset:128 nt
	v_addc_co_u32_e32 v11, vcc, 0, v229, vcc
	v_add_co_u32_e32 v14, vcc, 0x14c08000, v228
	s_nop 1
	v_addc_co_u32_e32 v15, vcc, 0, v229, vcc
	v_add_co_u32_e32 v18, vcc, 0x8810000, v228
	global_load_dwordx4 v[10:13], v[10:11], off offset:128
	s_nop 0
	global_load_dwordx4 v[14:17], v[14:15], off offset:128 nt
	v_addc_co_u32_e32 v19, vcc, 0, v229, vcc
	v_add_co_u32_e32 v22, vcc, 0x14c10000, v228
	s_nop 1
	v_addc_co_u32_e32 v23, vcc, 0, v229, vcc
	v_add_co_u32_e32 v26, vcc, 0x8818000, v228
	global_load_dwordx4 v[18:21], v[18:19], off offset:128
	s_nop 0
	global_load_dwordx4 v[22:25], v[22:23], off offset:128 nt
	v_addc_co_u32_e32 v27, vcc, 0, v229, vcc
	v_add_co_u32_e32 v30, vcc, 0x14c18000, v228
	s_nop 1
	v_addc_co_u32_e32 v31, vcc, 0, v229, vcc
	v_add_co_u32_e32 v34, vcc, 0x1400000, v226
	global_load_dwordx4 v[26:29], v[26:27], off offset:128
	s_nop 0
	global_load_dwordx4 v[30:33], v[30:31], off offset:128 nt
	v_addc_co_u32_e32 v35, vcc, 0, v227, vcc
	v_add_co_u32_e32 v38, vcc, 0x1420000, v226
	s_nop 1
	v_addc_co_u32_e32 v39, vcc, 0, v227, vcc
	v_add_co_u32_e32 v42, vcc, 0x1408000, v226
	global_load_dwordx4 v[34:37], v[34:35], off offset:128
	s_nop 0
	global_load_dwordx4 v[38:41], v[38:39], off offset:128
	v_addc_co_u32_e32 v43, vcc, 0, v227, vcc
	v_add_co_u32_e32 v46, vcc, 0x1428000, v226
	s_nop 1
	v_addc_co_u32_e32 v47, vcc, 0, v227, vcc
	v_add_co_u32_e32 v50, vcc, 0x1410000, v226
	global_load_dwordx4 v[42:45], v[42:43], off offset:128
	s_nop 0
	global_load_dwordx4 v[46:49], v[46:47], off offset:128
	v_addc_co_u32_e32 v51, vcc, 0, v227, vcc
	v_add_co_u32_e32 v54, vcc, 0x1430000, v226
	s_nop 1
	v_addc_co_u32_e32 v55, vcc, 0, v227, vcc
	v_add_co_u32_e32 v58, vcc, 0x1418000, v226
	global_load_dwordx4 v[50:53], v[50:51], off offset:128
	s_nop 0
	global_load_dwordx4 v[54:57], v[54:55], off offset:128
	v_addc_co_u32_e32 v59, vcc, 0, v227, vcc
	v_add_co_u32_e32 v62, vcc, 0x1438000, v226
	s_nop 1
	v_addc_co_u32_e32 v63, vcc, 0, v227, vcc
	global_load_dwordx4 v[58:61], v[58:59], off offset:128
	s_nop 0
	global_load_dwordx4 v[62:65], v[62:63], off offset:128
	s_waitcnt vmcnt(23)
	v_mfma_f32_16x16x32_bf16 v[94:97], v[142:145], v[162:165], v[94:97]
	s_add_i32 s20, s20, 2
	v_lshl_add_u64 v[224:225], v[224:225], 0, s[16:17]
	v_lshl_add_u64 v[222:223], v[222:223], 0, s[16:17]
	s_waitcnt vmcnt(21)
	v_mfma_f32_16x16x32_bf16 v[110:113], v[142:145], v[70:73], v[110:113]
	s_and_b64 vcc, exec, s[18:19]
	s_waitcnt vmcnt(19)
	v_mfma_f32_16x16x32_bf16 v[106:109], v[142:145], v[66:69], v[106:109]
	s_waitcnt vmcnt(17)
	v_mfma_f32_16x16x32_bf16 v[118:121], v[142:145], v[182:185], v[118:121]
	v_mfma_f32_16x16x32_bf16 v[94:97], v[146:149], v[162:165], v[94:97]
	v_mfma_f32_16x16x32_bf16 v[110:113], v[146:149], v[70:73], v[110:113]
	v_mfma_f32_16x16x32_bf16 v[106:109], v[146:149], v[66:69], v[106:109]
	v_mfma_f32_16x16x32_bf16 v[118:121], v[146:149], v[182:185], v[118:121]
	v_mfma_f32_16x16x32_bf16 v[94:97], v[142:145], v[166:169], v[94:97]
	v_mfma_f32_16x16x32_bf16 v[110:113], v[142:145], v[170:173], v[110:113]
	v_mfma_f32_16x16x32_bf16 v[106:109], v[142:145], v[178:181], v[106:109]
	s_waitcnt vmcnt(16)
	s_branch .Lrt_join_a

; #define GAS __attribute__((address_space(1)))
; __device__ __forceinline__ unsigned pk2(float lo, float hi) { return f2bf(lo) | (f2bf(hi) << 16); }
; #define NTLD(P) (NT_STREAMS ? __builtin_nontemporal_load(P) : *(P))
; __device__ __forceinline__ void phase_combine(Frame& F) {
;     ...
;     for (int t = gw; t < TL; t += NGW) {
;         const bf16* p = OC + (size_t)t * 2048 + h * 256 + e0;
;         const v4u a0 = NTLD((const GAS v4u*)p), a1 = NTLD((const GAS v4u*)(p + 8)), b0 = NTLD((const GAS v4u*)(p + 128)), b1 = NTLD((const GAS v4u*)(p + 136));
;         const unsigned aw[8] = {a0.x, a0.y, a0.z, a0.w, a1.x, a1.y, a1.z, a1.w}, bw[8] = {b0.x, b0.y, b0.z, b0.w, b1.x, b1.y, b1.z, b1.w};
;         float d[16]; float ss = 0.f;
; #pragma unroll
;         for (int i = 0; i < 8; ++i) { d[2 * i] = bf2f(aw[i] & 0xffffu) - lam * bf2f(bw[i] & 0xffffu); d[2 * i + 1] = bf2f(aw[i] >> 16) - lam * bf2f(bw[i] >> 16); ss += d[2 * i] * d[2 * i] + d[2 * i + 1] * d[2 * i + 1]; }
;         ss += __shfl_xor(ss, 1); ss += __shfl_xor(ss, 2); ss += __shfl_xor(ss, 4);
;         const float rstd = rsqrtf(ss * (1.f / 128.f) + EPSN);
;         unsigned w[8];
; #pragma unroll
;         for (int i = 0; i < 8; ++i) w[i] = pk2(d[2 * i] * rstd * sg[2 * i], d[2 * i + 1] * rstd * sg[2 * i + 1]);
;         bf16* q = AO + (size_t)t * DM + h * 128 + e0;
;         *(GAS v4u*)q = (v4u){w[0], w[1], w[2], w[3]}; *(GAS v4u*)(q + 8) = (v4u){w[4], w[5], w[6], w[7]};
;     }
.LBB0_1303:
	v_lshl_add_u64 v[30:31], v[6:7], 0, v[2:3]
	v_lshl_add_u64 v[48:49], v[30:31], 0, s[10:11]
	v_add_co_u32_e32 v50, vcc, 0x11000000, v30
	v_lshl_add_u64 v[52:53], v[30:31], 0, s[16:17]
	s_nop 0
	v_addc_co_u32_e32 v51, vcc, 0, v31, vcc
	global_load_dwordx4 v[30:33], v[48:49], off offset:16 nt
	global_load_dwordx4 v[34:37], v[52:53], off offset:16 nt
	global_load_dwordx4 v[38:41], v[50:51], off nt
	global_load_dwordx4 v[42:45], v[50:51], off offset:256 nt
	v_lshl_add_u64 v[102:103], v[50:51], 0, s[14:15]
	global_load_dword v100, v[102:103], off
	global_load_dword v101, v[102:103], off offset:256
	v_lshl_add_u64 v[46:47], v[4:5], 0, v[2:3]
	v_add_co_u32_e32 v46, vcc, 0xcc00000, v46
	s_add_i32 s4, s4, s2
	s_nop 0
	v_addc_co_u32_e32 v47, vcc, 0, v47, vcc
	v_lshl_add_u64 v[4:5], v[4:5], 0, s[12:13]
	v_lshl_add_u64 v[6:7], v[6:7], 0, s[14:15]
	s_cmp_lt_i32 s4, 0x8000
	s_waitcnt vmcnt(5)
	v_lshlrev_b32_e32 v49, 16, v31
	v_lshlrev_b32_e32 v48, 16, v30
	s_waitcnt vmcnt(3)
	v_lshlrev_b32_e32 v57, 16, v39
	v_lshlrev_b32_e32 v56, 16, v38
	s_waitcnt vmcnt(2)
	v_lshlrev_b32_e32 v59, 16, v43
	v_lshlrev_b32_e32 v58, 16, v42
	v_and_b32_e32 v39, 0xffff0000, v39
	v_and_b32_e32 v38, 0xffff0000, v38
	v_and_b32_e32 v43, 0xffff0000, v43
	v_and_b32_e32 v42, 0xffff0000, v42
	v_lshlrev_b32_e32 v51, 16, v35
	v_lshlrev_b32_e32 v50, 16, v34
	v_and_b32_e32 v31, 0xffff0000, v31
	v_and_b32_e32 v30, 0xffff0000, v30
	v_and_b32_e32 v35, 0xffff0000, v35
	v_and_b32_e32 v34, 0xffff0000, v34
	v_lshlrev_b32_e32 v53, 16, v33
	v_lshlrev_b32_e32 v52, 16, v32
	v_lshlrev_b32_e32 v55, 16, v37
	v_lshlrev_b32_e32 v54, 16, v36
	v_and_b32_e32 v33, 0xffff0000, v33
	v_and_b32_e32 v32, 0xffff0000, v32
	v_and_b32_e32 v37, 0xffff0000, v37
	v_and_b32_e32 v36, 0xffff0000, v36
	v_lshlrev_b32_e32 v61, 16, v41
	v_lshlrev_b32_e32 v60, 16, v40
	v_lshlrev_b32_e32 v63, 16, v45
	v_lshlrev_b32_e32 v62, 16, v44
	v_and_b32_e32 v41, 0xffff0000, v41
	v_and_b32_e32 v40, 0xffff0000, v40
	v_and_b32_e32 v45, 0xffff0000, v45
	v_and_b32_e32 v44, 0xffff0000, v44
	v_pk_fma_f32 v[38:39], v[8:9], v[42:43], v[38:39] neg_lo:[1,0,0] neg_hi:[1,0,0]
	v_pk_fma_f32 v[30:31], v[8:9], v[34:35], v[30:31] neg_lo:[1,0,0] neg_hi:[1,0,0]
	v_pk_fma_f32 v[34:35], v[8:9], v[54:55], v[52:53] neg_lo:[1,0,0] neg_hi:[1,0,0]
	v_pk_fma_f32 v[32:33], v[8:9], v[36:37], v[32:33] neg_lo:[1,0,0] neg_hi:[1,0,0]
	v_pk_fma_f32 v[36:37], v[8:9], v[58:59], v[56:57] neg_lo:[1,0,0] neg_hi:[1,0,0]
	v_pk_fma_f32 v[40:41], v[8:9], v[44:45], v[40:41] neg_lo:[1,0,0] neg_hi:[1,0,0]
	v_pk_mul_f32 v[52:53], v[38:39], v[38:39]
	v_pk_fma_f32 v[42:43], v[8:9], v[62:63], v[60:61] neg_lo:[1,0,0] neg_hi:[1,0,0]
	v_pk_mul_f32 v[54:55], v[40:41], v[40:41]
	v_pk_fma_f32 v[52:53], v[36:37], v[36:37], v[52:53]
	v_pk_fma_f32 v[54:55], v[42:43], v[42:43], v[54:55]
	v_add_f32_e32 v29, v52, v53
	v_pk_fma_f32 v[48:49], v[8:9], v[50:51], v[48:49] neg_lo:[1,0,0] neg_hi:[1,0,0]
	v_pk_mul_f32 v[44:45], v[30:31], v[30:31]
	v_add_f32_e32 v29, v54, v29
	v_pk_fma_f32 v[44:45], v[48:49], v[48:49], v[44:45]
	v_add_f32_e32 v29, v55, v29
	v_pk_mul_f32 v[50:51], v[32:33], v[32:33]
	v_add_f32_e32 v29, v44, v29
	v_pk_fma_f32 v[50:51], v[34:35], v[34:35], v[50:51]
	v_add_f32_e32 v29, v45, v29
	v_add_f32_e32 v29, v50, v29
	v_add_f32_e32 v29, v51, v29
	ds_bpermute_b32 v44, v1, v29
	s_waitcnt lgkmcnt(0)
	v_add_f32_e32 v29, v29, v44
	ds_bpermute_b32 v44, v26, v29
	s_waitcnt lgkmcnt(0)
	v_add_f32_e32 v29, v29, v44
	ds_bpermute_b32 v44, v27, v29
	s_waitcnt lgkmcnt(0)
	v_add_f32_e32 v29, v29, v44
	v_fmamk_f32 v29, v29, 0x3c000000, v28
	v_mul_f32_e32 v44, 0x4b800000, v29
	v_cmp_gt_f32_e32 vcc, s5, v29
	s_nop 1
	v_cndmask_b32_e32 v29, v29, v44, vcc
	v_rsq_f32_e32 v29, v29
	s_nop 0
	v_mul_f32_e32 v44, 0x45800000, v29
	v_cndmask_b32_e32 v44, v29, v44, vcc
	v_pk_mul_f32 v[36:37], v[36:37], v[44:45] op_sel_hi:[1,0]
	v_pk_mul_f32 v[42:43], v[42:43], v[44:45] op_sel_hi:[1,0]
	v_pk_mul_f32 v[40:41], v[40:41], v[44:45] op_sel_hi:[1,0]
	v_pk_mul_f32 v[38:39], v[38:39], v[44:45] op_sel_hi:[1,0]
	v_pk_mul_f32 v[48:49], v[48:49], v[44:45] op_sel_hi:[1,0]
	v_pk_mul_f32 v[30:31], v[30:31], v[44:45] op_sel_hi:[1,0]
	v_pk_mul_f32 v[34:35], v[34:35], v[44:45] op_sel_hi:[1,0]
	v_pk_mul_f32 v[32:33], v[32:33], v[44:45] op_sel_hi:[1,0]
	v_pk_mul_f32 v[36:37], v[10:11], v[36:37]
	v_pk_mul_f32 v[42:43], v[14:15], v[42:43]
	v_pk_mul_f32 v[40:41], v[16:17], v[40:41]
	v_pk_mul_f32 v[38:39], v[12:13], v[38:39]
	v_pk_mul_f32 v[44:45], v[18:19], v[48:49]
	v_pk_mul_f32 v[30:31], v[20:21], v[30:31]
	v_pk_mul_f32 v[34:35], v[22:23], v[34:35]
	v_pk_mul_f32 v[32:33], v[24:25], v[32:33]
	v_bfe_u32 v29, v41, 16, 1
	v_bfe_u32 v51, v36, 16, 1
	v_bfe_u32 v52, v37, 16, 1
	v_bfe_u32 v53, v42, 16, 1
	v_bfe_u32 v54, v43, 16, 1
	v_bfe_u32 v48, v40, 16, 1
	v_bfe_u32 v49, v39, 16, 1
	v_bfe_u32 v50, v38, 16, 1
	v_bfe_u32 v55, v33, 16, 1
	v_bfe_u32 v56, v32, 16, 1
	v_bfe_u32 v57, v31, 16, 1
	v_bfe_u32 v58, v30, 16, 1
	v_bfe_u32 v59, v44, 16, 1
	v_bfe_u32 v60, v45, 16, 1
	v_bfe_u32 v61, v34, 16, 1
	v_bfe_u32 v62, v35, 16, 1
	v_add3_u32 v29, v41, v29, s18
	v_add3_u32 v41, v43, v54, s18
	v_add3_u32 v42, v42, v53, s18
	v_add3_u32 v37, v37, v52, s18
	v_add3_u32 v36, v36, v51, s18
	v_add3_u32 v38, v38, v50, s18
	v_add3_u32 v39, v39, v49, s18
	v_add3_u32 v40, v40, v48, s18
	v_add3_u32 v43, v30, v58, s18
	v_add3_u32 v48, v31, v57, s18
	v_add3_u32 v49, v32, v56, s18
	v_add3_u32 v50, v33, v55, s18
	v_add3_u32 v30, v35, v62, s18
	v_add3_u32 v31, v34, v61, s18
	v_add3_u32 v32, v45, v60, s18
	v_add3_u32 v33, v44, v59, s18
	v_lshrrev_b32_e32 v34, 16, v36
	v_lshrrev_b32_e32 v35, 16, v37
	v_lshrrev_b32_e32 v36, 16, v42
	v_lshrrev_b32_e32 v37, 16, v41
	v_lshrrev_b32_e32 v41, 16, v33
	v_lshrrev_b32_e32 v42, 16, v32
	v_lshrrev_b32_e32 v44, 16, v31
	v_lshrrev_b32_e32 v45, 16, v30
	v_and_or_b32 v33, v29, s3, v37
	v_and_or_b32 v32, v40, s3, v36
	v_and_or_b32 v31, v39, s3, v35
	v_and_or_b32 v30, v38, s3, v34
	v_and_or_b32 v37, v50, s3, v45
	v_and_or_b32 v36, v49, s3, v44
	v_and_or_b32 v35, v48, s3, v42
	v_and_or_b32 v34, v43, s3, v41
	global_store_dwordx4 v[46:47], v[30:33], off
	global_store_dwordx4 v[46:47], v[34:37], off offset:16
	s_cbranch_scc1 .LBB0_1303

;     ...
;         bf16x8 xhA[4], xlA[4], whA[4], wlA[4], xhB[4], xlB[4], whB[4], wlB[4];
;         RT_LOAD(xhA, xlA, whA, wlA, 0);
;         for (int ks = 0; ks < 32; ks += 2) {
;             RT_LOAD(xhB, xlB, whB, wlB, (ks + 1) * 32);
;             RT_MMA(xhA, xlA, whA, wlA);
;             if (ks + 2 < 32) RT_LOAD(xhA, xlA, whA, wlA, (ks + 2) * 32);
;             RT_MMA(xhB, xlB, whB, wlB);
;         }
.LBB0_1512:
	v_lshl_add_u64 v[228:229], s[38:39], 0, v[222:223]
	v_add_co_u32_e32 v130, vcc, s43, v228
	v_lshl_add_u64 v[226:227], s[38:39], 0, v[224:225]
	s_nop 0
	v_addc_co_u32_e32 v131, vcc, 0, v229, vcc
	v_add_co_u32_e32 v132, vcc, s44, v228
	s_waitcnt vmcnt(0)
	v_mfma_f32_16x16x32_bf16 v[182:185], v[26:29], v[50:53], v[66:69]
	v_addc_co_u32_e32 v133, vcc, 0, v229, vcc
	global_load_dwordx4 v[154:157], v[130:131], off offset:64
	global_load_dwordx4 v[158:161], v[132:133], off offset:64 nt
	v_add_co_u32_e32 v130, vcc, s45, v228
	v_mfma_f32_16x16x32_bf16 v[70:73], v[26:29], v[42:45], v[70:73]
	s_nop 0
	v_addc_co_u32_e32 v131, vcc, 0, v229, vcc
	v_add_co_u32_e32 v132, vcc, s46, v228
	v_mfma_f32_16x16x32_bf16 v[182:185], v[30:33], v[50:53], v[182:185]
	s_nop 0
	v_addc_co_u32_e32 v133, vcc, 0, v229, vcc
	v_add_co_u32_e32 v134, vcc, s47, v228
	global_load_dwordx4 v[142:145], v[130:131], off offset:64
	global_load_dwordx4 v[146:149], v[132:133], off offset:64 nt
	v_addc_co_u32_e32 v135, vcc, 0, v229, vcc
	v_add_co_u32_e32 v136, vcc, s48, v228
	v_mfma_f32_16x16x32_bf16 v[130:133], v[18:21], v[58:61], v[90:93]
	s_nop 0
	v_addc_co_u32_e32 v137, vcc, 0, v229, vcc
	s_nop 0
	global_load_dwordx4 v[90:93], v[134:135], off offset:64
	global_load_dwordx4 v[138:141], v[136:137], off offset:64 nt
	v_add_co_u32_e32 v134, vcc, s49, v228
	v_mfma_f32_16x16x32_bf16 v[130:133], v[22:25], v[58:61], v[130:133]
	s_nop 0
	v_addc_co_u32_e32 v135, vcc, 0, v229, vcc
	v_add_co_u32_e32 v136, vcc, s50, v228
	v_mfma_f32_16x16x32_bf16 v[150:153], v[18:21], v[62:65], v[130:133]
	s_nop 0
	v_addc_co_u32_e32 v137, vcc, 0, v229, vcc
	v_add_co_u32_e32 v162, vcc, s51, v226
	s_nop 0
	global_load_dwordx4 v[130:133], v[134:135], off offset:64
	s_nop 0
	global_load_dwordx4 v[134:137], v[136:137], off offset:64 nt
	v_addc_co_u32_e32 v163, vcc, 0, v227, vcc
	v_add_co_u32_e32 v166, vcc, s52, v226
	v_mfma_f32_16x16x32_bf16 v[174:177], v[30:33], v[42:45], v[70:73]
	s_nop 0
	v_addc_co_u32_e32 v167, vcc, 0, v227, vcc
	v_add_co_u32_e32 v170, vcc, s53, v226
	global_load_dwordx4 v[162:165], v[162:163], off offset:64
	s_nop 0
	global_load_dwordx4 v[166:169], v[166:167], off offset:64
	v_addc_co_u32_e32 v171, vcc, 0, v227, vcc
	v_add_co_u32_e32 v172, vcc, s54, v226
	v_mfma_f32_16x16x32_bf16 v[186:189], v[26:29], v[54:57], v[182:185]
	s_nop 0
	v_addc_co_u32_e32 v173, vcc, 0, v227, vcc
	v_add_co_u32_e32 v178, vcc, s55, v226
	global_load_dwordx4 v[70:73], v[170:171], off offset:64
	s_nop 0
	global_load_dwordx4 v[170:173], v[172:173], off offset:64
	v_addc_co_u32_e32 v179, vcc, 0, v227, vcc
	v_add_co_u32_e32 v180, vcc, s56, v226
	v_mfma_f32_16x16x32_bf16 v[190:193], v[26:29], v[58:61], v[126:129]
	s_nop 0
	v_addc_co_u32_e32 v181, vcc, 0, v227, vcc
	v_add_co_u32_e32 v238, vcc, s57, v226
	global_load_dwordx4 v[66:69], v[178:179], off offset:64
	s_nop 0
	global_load_dwordx4 v[178:181], v[180:181], off offset:64
	v_addc_co_u32_e32 v239, vcc, 0, v227, vcc
	v_add_co_u32_e32 v240, vcc, s58, v226
	v_mfma_f32_16x16x32_bf16 v[78:81], v[2:5], v[34:37], v[78:81]
	s_nop 0
	v_addc_co_u32_e32 v241, vcc, 0, v227, vcc
	global_load_dwordx4 v[182:185], v[238:239], off offset:64
	global_load_dwordx4 v[126:129], v[240:241], off offset:64
	v_mfma_f32_16x16x32_bf16 v[82:85], v[2:5], v[42:45], v[82:85]
	s_cmp_gt_u32 s18, 29
	s_cselect_b64 s[16:17], -1, 0
	s_and_b64 vcc, exec, s[16:17]
	v_mfma_f32_16x16x32_bf16 v[86:89], v[2:5], v[50:53], v[86:89]
	v_mfma_f32_16x16x32_bf16 v[98:101], v[2:5], v[58:61], v[98:101]
	v_mfma_f32_16x16x32_bf16 v[94:97], v[10:13], v[34:37], v[94:97]
	v_mfma_f32_16x16x32_bf16 v[110:113], v[10:13], v[42:45], v[110:113]
	v_mfma_f32_16x16x32_bf16 v[106:109], v[10:13], v[50:53], v[106:109]
	v_mfma_f32_16x16x32_bf16 v[118:121], v[10:13], v[58:61], v[118:121]
	v_mfma_f32_16x16x32_bf16 v[114:117], v[18:21], v[34:37], v[114:117]
	v_mfma_f32_16x16x32_bf16 v[122:125], v[18:21], v[42:45], v[122:125]
	v_mfma_f32_16x16x32_bf16 v[102:105], v[18:21], v[50:53], v[102:105]
	v_mfma_f32_16x16x32_bf16 v[74:77], v[26:29], v[34:37], v[74:77]
	v_mfma_f32_16x16x32_bf16 v[78:81], v[6:9], v[34:37], v[78:81]
	v_mfma_f32_16x16x32_bf16 v[82:85], v[6:9], v[42:45], v[82:85]
	v_mfma_f32_16x16x32_bf16 v[86:89], v[6:9], v[50:53], v[86:89]
	v_mfma_f32_16x16x32_bf16 v[98:101], v[6:9], v[58:61], v[98:101]
	v_mfma_f32_16x16x32_bf16 v[94:97], v[14:17], v[34:37], v[94:97]
	v_mfma_f32_16x16x32_bf16 v[110:113], v[14:17], v[42:45], v[110:113]
	v_mfma_f32_16x16x32_bf16 v[106:109], v[14:17], v[50:53], v[106:109]
	v_mfma_f32_16x16x32_bf16 v[118:121], v[14:17], v[58:61], v[118:121]
	v_mfma_f32_16x16x32_bf16 v[114:117], v[22:25], v[34:37], v[114:117]
	v_mfma_f32_16x16x32_bf16 v[122:125], v[22:25], v[42:45], v[122:125]
	v_mfma_f32_16x16x32_bf16 v[102:105], v[22:25], v[50:53], v[102:105]
	v_mfma_f32_16x16x32_bf16 v[74:77], v[30:33], v[34:37], v[74:77]
	v_mfma_f32_16x16x32_bf16 v[190:193], v[30:33], v[58:61], v[190:193]
	v_mfma_f32_16x16x32_bf16 v[78:81], v[2:5], v[38:41], v[78:81]
	v_mfma_f32_16x16x32_bf16 v[82:85], v[2:5], v[46:49], v[82:85]
	v_mfma_f32_16x16x32_bf16 v[86:89], v[2:5], v[54:57], v[86:89]
	v_mfma_f32_16x16x32_bf16 v[98:101], v[2:5], v[62:65], v[98:101]
	v_mfma_f32_16x16x32_bf16 v[94:97], v[10:13], v[38:41], v[94:97]
	v_mfma_f32_16x16x32_bf16 v[110:113], v[10:13], v[46:49], v[110:113]
	v_mfma_f32_16x16x32_bf16 v[106:109], v[10:13], v[54:57], v[106:109]
	v_mfma_f32_16x16x32_bf16 v[118:121], v[10:13], v[62:65], v[118:121]
	v_mfma_f32_16x16x32_bf16 v[114:117], v[18:21], v[38:41], v[114:117]
	v_mfma_f32_16x16x32_bf16 v[122:125], v[18:21], v[46:49], v[122:125]
	v_mfma_f32_16x16x32_bf16 v[102:105], v[18:21], v[54:57], v[102:105]
	v_mfma_f32_16x16x32_bf16 v[74:77], v[26:29], v[38:41], v[74:77]
	v_mfma_f32_16x16x32_bf16 v[174:177], v[26:29], v[46:49], v[174:177]
	v_mfma_f32_16x16x32_bf16 v[190:193], v[26:29], v[62:65], v[190:193]
	s_cbranch_vccnz .LBB0_1511
;     ...
;         bf16x8 xhA[4], xlA[4], whA[4], wlA[4], xhB[4], xlB[4], whB[4], wlB[4];
;         RT_LOAD(xhA, xlA, whA, wlA, 0);
;         for (int ks = 0; ks < 32; ks += 2) {
;             RT_LOAD(xhB, xlB, whB, wlB, (ks + 1) * 32);
;             RT_MMA(xhA, xlA, whA, wlA);
;             if (ks + 2 < 32) RT_LOAD(xhA, xlA, whA, wlA, (ks + 2) * 32);
;             RT_MMA(xhB, xlB, whB, wlB);
;         }
	v_add_co_u32_e32 v2, vcc, 0x8800000, v228
	s_nop 1
	v_addc_co_u32_e32 v3, vcc, 0, v229, vcc
	v_add_co_u32_e32 v6, vcc, 0x14c00000, v228
	s_nop 1
	v_addc_co_u32_e32 v7, vcc, 0, v229, vcc
	v_add_co_u32_e32 v10, vcc, 0x8808000, v228
	global_load_dwordx4 v[2:5], v[2:3], off offset:128
	s_nop 0
	global_load_dwordx4 v[6:9], v[6:7], off offset:128 nt
	v_addc_co_u32_e32 v11, vcc, 0, v229, vcc
	v_add_co_u32_e32 v14, vcc, 0x14c08000, v228
	s_nop 1
	v_addc_co_u32_e32 v15, vcc, 0, v229, vcc
	v_add_co_u32_e32 v18, vcc, 0x8810000, v228
	global_load_dwordx4 v[10:13], v[10:11], off offset:128
	s_nop 0
	global_load_dwordx4 v[14:17], v[14:15], off offset:128 nt
	v_addc_co_u32_e32 v19, vcc, 0, v229, vcc
	v_add_co_u32_e32 v22, vcc, 0x14c10000, v228
	s_nop 1
	v_addc_co_u32_e32 v23, vcc, 0, v229, vcc
	v_add_co_u32_e32 v26, vcc, 0x8818000, v228
	global_load_dwordx4 v[18:21], v[18:19], off offset:128
	s_nop 0
	global_load_dwordx4 v[22:25], v[22:23], off offset:128 nt
	v_addc_co_u32_e32 v27, vcc, 0, v229, vcc
	v_add_co_u32_e32 v30, vcc, 0x14c18000, v228
	s_nop 1
	v_addc_co_u32_e32 v31, vcc, 0, v229, vcc
	v_add_co_u32_e32 v34, vcc, 0x1440000, v226
	global_load_dwordx4 v[26:29], v[26:27], off offset:128
	s_nop 0
	global_load_dwordx4 v[30:33], v[30:31], off offset:128 nt
	v_addc_co_u32_e32 v35, vcc, 0, v227, vcc
	v_add_co_u32_e32 v38, vcc, 0x1460000, v226
	s_nop 1
	v_addc_co_u32_e32 v39, vcc, 0, v227, vcc
	v_add_co_u32_e32 v42, vcc, 0x1448000, v226
	global_load_dwordx4 v[34:37], v[34:35], off offset:128
	s_nop 0
	global_load_dwordx4 v[38:41], v[38:39], off offset:128
	v_addc_co_u32_e32 v43, vcc, 0, v227, vcc
	v_add_co_u32_e32 v46, vcc, 0x1468000, v226
	s_nop 1
	v_addc_co_u32_e32 v47, vcc, 0, v227, vcc
	v_add_co_u32_e32 v50, vcc, 0x1450000, v226
	global_load_dwordx4 v[42:45], v[42:43], off offset:128
	s_nop 0
	global_load_dwordx4 v[46:49], v[46:47], off offset:128
	v_addc_co_u32_e32 v51, vcc, 0, v227, vcc
	v_add_co_u32_e32 v54, vcc, 0x1470000, v226
	s_nop 1
	v_addc_co_u32_e32 v55, vcc, 0, v227, vcc
	v_add_co_u32_e32 v58, vcc, 0x1458000, v226
	global_load_dwordx4 v[50:53], v[50:51], off offset:128
	s_nop 0
	global_load_dwordx4 v[54:57], v[54:55], off offset:128
	v_addc_co_u32_e32 v59, vcc, 0, v227, vcc
	v_add_co_u32_e32 v62, vcc, 0x1478000, v226
	s_nop 1
	v_addc_co_u32_e32 v63, vcc, 0, v227, vcc
	global_load_dwordx4 v[58:61], v[58:59], off offset:128
	s_nop 0
	global_load_dwordx4 v[62:65], v[62:63], off offset:128
	s_waitcnt vmcnt(23)
	v_mfma_f32_16x16x32_bf16 v[94:97], v[142:145], v[162:165], v[94:97]
	s_add_i32 s18, s18, 2
	v_lshl_add_u64 v[224:225], v[224:225], 0, s[14:15]
	v_lshl_add_u64 v[222:223], v[222:223], 0, s[14:15]
	s_waitcnt vmcnt(21)
	v_mfma_f32_16x16x32_bf16 v[110:113], v[142:145], v[70:73], v[110:113]
	s_and_b64 vcc, exec, s[16:17]
	s_waitcnt vmcnt(19)
	v_mfma_f32_16x16x32_bf16 v[106:109], v[142:145], v[66:69], v[106:109]
	s_waitcnt vmcnt(17)
	v_mfma_f32_16x16x32_bf16 v[118:121], v[142:145], v[182:185], v[118:121]
	v_mfma_f32_16x16x32_bf16 v[94:97], v[146:149], v[162:165], v[94:97]
	v_mfma_f32_16x16x32_bf16 v[110:113], v[146:149], v[70:73], v[110:113]
	v_mfma_f32_16x16x32_bf16 v[106:109], v[146:149], v[66:69], v[106:109]
	v_mfma_f32_16x16x32_bf16 v[118:121], v[146:149], v[182:185], v[118:121]
	v_mfma_f32_16x16x32_bf16 v[94:97], v[142:145], v[166:169], v[94:97]
	v_mfma_f32_16x16x32_bf16 v[110:113], v[142:145], v[170:173], v[110:113]
	v_mfma_f32_16x16x32_bf16 v[106:109], v[142:145], v[178:181], v[106:109]
	s_waitcnt vmcnt(16)
	s_branch .Lrt_join_b
